# fp8 GEMM LDS fragment reads made bank-conflict-free (odd-fq lanes swap their two 16B K pieces, same for A and B)
# speedup vs baseline: 1.0276x; 1.0276x over previous
; #define GAS __attribute__((address_space(1)))
; #define PG8_STAGE(bufoff, gbase, voff) do { _Pragma("unroll") for (int _i = 0; _i < 2; ++_i) \
;         __builtin_amdgcn_global_load_lds((const GAS unsigned*)((const GAS char*)(gbase) + (voff)[_i]), (LAS unsigned*)(lds + (bufoff) + ldsw + _i * 8192), 16, 0, 0); } while (0)
; #define PG8_WAIT_V(n) asm volatile("s_waitcnt vmcnt(" #n ")" ::: "memory")
; #define PG8_BAR __builtin_amdgcn_s_barrier()
; #define PG8_OFFS(u, ao, bo) do { _Pragma("unroll") for (int _i = 0; _i < 2; ++_i) { (bo)[_i] = (unsigned)(sRb[_i] * (u).ldb + sC2[_i]); \
;         _Pragma("unroll") for (int _h = 0; _h < 2; ++_h) { int _r = _h * HALF + sR[_i]; if (GATHER) { _r = (u).gl ? (u).gl[_r] : ((_r < (u).gcnt) ? (u).gidx[_r] : 0); } (ao)[_h][_i] = (unsigned)(_r * (u).lda + sC2[_i]); } } } while (0)
; template <class Epi, class Sched, bool GATHER, bool FP8 = false, bool UNI = false>
; __device__ __forceinline__ void gemm_phase(LAS unsigned char* lds, const Sched& S, const Epi& E) {
;     ...
;     const int aoff = lds_byte(wr * 64 + fr, fq * 8), boff = lds_byte(wc * 32 + fr, fq * 8);
;     const int sclw = 0x79, scla = 0x7f;
;     const int aoff8[2] = {lds_byte(wr * 64 + fr, fq * 16), lds_byte(wr * 64 + fr, fq * 16 + 8)}, boff8[2] = {lds_byte(wc * 32 + fr, fq * 16), lds_byte(wc * 32 + fr, fq * 16 + 8)};
;     ...
;     Unit cur, nxt; int ui = 0;
;     if (!S.next(0, cur)) return;
;     f32x4 acc[2][2][4][2];
; #pragma unroll
;     for (int a = 0; a < 2; ++a)
; #pragma unroll
;         for (int b = 0; b < 2; ++b)
; #pragma unroll
;             for (int m = 0; m < 4; ++m)
; #pragma unroll
;                 for (int n = 0; n < 2; ++n) acc[a][b][m][n] = (f32x4){0.f, 0.f, 0.f, 0.f};
;     i32x8 At[4], B0[2], B1[2];
;     unsigned aoc[2][2], boc[2], aon[2][2], bon[2];
;     PG8_OFFS(cur, aoc, boc);
;     {
;         const GAS char* cA = cur.a; const GAS char* cB = cur.b; const size_t hB = (size_t)(Epi::WIDE ? 32 : HALF) * cur.ldb;
;         PG8_STAGE(PG8_SB(0, 0), cB, boc); PG8_STAGE(PG8_SB(0, 1), cB + hB, boc); PG8_STAGE(PG8_SA(0, 0), cA, aoc[0]); PG8_STAGE(PG8_SA(0, 1), cA, aoc[1]);
;         if (wr == 1) PG8_BAR;
;         PG8_WAIT_V(2); PG8_BAR;
;         PG8_STAGE(PG8_SB(1, 0), cB + 128, boc); PG8_STAGE(PG8_SA(1, 0), cA + 128, aoc[0]); PG8_STAGE(PG8_SB(1, 1), cB + hB + 128, boc);
;         PG8_WAIT_V(6); PG8_BAR;
.LBB0_312:
	s_add_i32 s51, s56, s14
	v_lshl_add_u64 v[8:9], v[8:9], 0, s[74:75]
	s_mov_b32 m0, s51
	s_add_i32 s24, s51, 0x2000
	s_and_b32 s1, s1, 3
	s_waitcnt vmcnt(2)
	s_barrier
	global_load_lds_dwordx4 v[8:9], off
	v_lshl_add_u64 v[6:7], v[6:7], 0, s[74:75]
	s_mov_b32 m0, s24
	s_add_i32 s25, s86, 0x8000
	s_add_i32 s60, s86, 0xa000
	global_load_lds_dwordx4 v[6:7], off
	v_lshl_add_u64 v[2:3], v[2:3], 0, s[74:75]
	s_mov_b32 m0, s25
	s_add_u32 s16, s8, 0x40080
	global_load_lds_dwordx4 v[2:3], off
	v_lshl_add_u64 v[2:3], v[4:5], 0, s[74:75]
	s_mov_b32 m0, s60
	s_addc_u32 s17, s9, 0
	s_add_i32 s61, s57, s14
	global_load_lds_dwordx4 v[2:3], off
	v_lshl_add_u64 v[2:3], s[16:17], 0, v[166:167]
	s_mov_b32 m0, s61
	s_add_i32 s58, s61, 0x2000
	global_load_lds_dwordx4 v[2:3], off
	v_lshl_add_u64 v[2:3], s[16:17], 0, v[172:173]
	s_mov_b32 m0, s58
	v_bfe_u32 v18, v16, 4, 2
	global_load_lds_dwordx4 v[2:3], off
	v_lshlrev_b32_e32 v2, 14, v13
	v_and_b32_e32 v2, 0xffff8000, v2
	v_lshl_add_u32 v2, v14, 11, v2
	v_and_b32_e32 v3, 1, v13
	v_and_b32_e32 v17, 15, v16
	v_lshlrev_b32_e32 v19, 3, v18
	v_lshlrev_b32_e32 v18, 5, v18
	v_lshl_or_b32 v2, v3, 6, v2
	v_lshlrev_b32_e32 v3, 1, v15
	v_lshl_or_b32 v198, s15, 6, v17
	v_lshlrev_b32_e32 v17, 6, v17
	v_lshlrev_b32_e32 v20, 2, v16
	v_and_b32_e32 v21, 32, v18
	v_lshlrev_b32_e32 v16, 5, v16
	v_add3_u32 v184, v2, v3, s62
	v_lshlrev_b32_e32 v2, 14, v10
	v_and_b32_e32 v20, 32, v20
	v_or_b32_e32 v22, v17, v21
	v_and_b32_e32 v16, 0x400, v16
	v_and_b32_e32 v2, 0xffff8000, v2
	v_lshl_or_b32 v23, s15, 13, v16
	v_bitop3_b32 v17, v17, v20, v21 bitop3:0x36
	v_bitop3_b32 v20, v22, v20, 16 bitop3:0x36
	s_waitcnt vmcnt(6)
	v_lshl_or_b32 v178, s1, 5, v19
	v_lshl_or_b32 v162, s1, 7, v18
	v_lshl_add_u32 v2, v11, 11, v2
	v_and_b32_e32 v3, 1, v10
	v_or_b32_e32 v21, v17, v23
	v_or_b32_e32 v22, v20, v23
	v_lshl_or_b32 v16, s1, 12, v16
	s_cmpk_lt_u32 s0, 0x100
	v_lshl_add_u64 v[180:181], s[36:37], 0, v[162:163]
	v_lshlrev_b32_e32 v162, 2, v178
	v_lshl_or_b32 v2, v3, 6, v2
	v_lshlrev_b32_e32 v3, 1, v12
	v_mov_b32_e32 v171, v163
	v_mov_b32_e32 v177, v163
	v_or_b32_e32 v199, v17, v16
	v_or_b32_e32 v200, v20, v16
	s_cselect_b64 s[14:15], -1, 0
	v_lshl_add_u64 v[182:183], s[34:35], 0, v[162:163]
	v_mov_b32_e32 v185, v163
	v_add3_u32 v186, v2, v3, s62
	v_mov_b32_e32 v187, v163
	s_mov_b32 s59, 0
	v_add_u32_e32 v201, s3, v21
	v_add_u32_e32 v202, s3, v22
	v_mbcnt_lo_u32_b32 v255, -1, 0
	v_mbcnt_hi_u32_b32 v255, -1, v255
	v_and_b32_e32 v255, 16, v255
	v_xor_b32_e32 v199, v199, v255
	v_xor_b32_e32 v200, v200, v255
	v_xor_b32_e32 v201, v201, v255
	v_xor_b32_e32 v202, v202, v255
	s_barrier
	s_branch .LBB0_315

; #define GAS __attribute__((address_space(1)))
; #define PG8_STAGE(bufoff, gbase, voff) do { _Pragma("unroll") for (int _i = 0; _i < 2; ++_i) \
;         __builtin_amdgcn_global_load_lds((const GAS unsigned*)((const GAS char*)(gbase) + (voff)[_i]), (LAS unsigned*)(lds + (bufoff) + ldsw + _i * 8192), 16, 0, 0); } while (0)
; #define PG8_WAIT_V(n) asm volatile("s_waitcnt vmcnt(" #n ")" ::: "memory")
; #define PG8_BAR __builtin_amdgcn_s_barrier()
; #define PG8_OFFS(u, ao, bo) do { _Pragma("unroll") for (int _i = 0; _i < 2; ++_i) { (bo)[_i] = (unsigned)(sRb[_i] * (u).ldb + sC2[_i]); \
;         _Pragma("unroll") for (int _h = 0; _h < 2; ++_h) { int _r = _h * HALF + sR[_i]; if (GATHER) { _r = (u).gl ? (u).gl[_r] : ((_r < (u).gcnt) ? (u).gidx[_r] : 0); } (ao)[_h][_i] = (unsigned)(_r * (u).lda + sC2[_i]); } } } while (0)
; template <class Epi, class Sched, bool GATHER, bool FP8 = false, bool UNI = false>
; __device__ __forceinline__ void gemm_phase(LAS unsigned char* lds, const Sched& S, const Epi& E) {
;     ...
;     const int aoff = lds_byte(wr * 64 + fr, fq * 8), boff = lds_byte(wc * 32 + fr, fq * 8);
;     const int sclw = 0x79, scla = 0x7f;
;     const int aoff8[2] = {lds_byte(wr * 64 + fr, fq * 16), lds_byte(wr * 64 + fr, fq * 16 + 8)}, boff8[2] = {lds_byte(wc * 32 + fr, fq * 16), lds_byte(wc * 32 + fr, fq * 16 + 8)};
;     ...
;     Unit cur, nxt; int ui = 0;
;     if (!S.next(0, cur)) return;
;     f32x4 acc[2][2][4][2];
; #pragma unroll
;     for (int a = 0; a < 2; ++a)
; #pragma unroll
;         for (int b = 0; b < 2; ++b)
; #pragma unroll
;             for (int m = 0; m < 4; ++m)
; #pragma unroll
;                 for (int n = 0; n < 2; ++n) acc[a][b][m][n] = (f32x4){0.f, 0.f, 0.f, 0.f};
;     i32x8 At[4], B0[2], B1[2];
;     unsigned aoc[2][2], boc[2], aon[2][2], bon[2];
;     PG8_OFFS(cur, aoc, boc);
;     {
;         const GAS char* cA = cur.a; const GAS char* cB = cur.b; const size_t hB = (size_t)(Epi::WIDE ? 32 : HALF) * cur.ldb;
;         PG8_STAGE(PG8_SB(0, 0), cB, boc); PG8_STAGE(PG8_SB(0, 1), cB + hB, boc); PG8_STAGE(PG8_SA(0, 0), cA, aoc[0]); PG8_STAGE(PG8_SA(0, 1), cA, aoc[1]);
;         if (wr == 1) PG8_BAR;
;         PG8_WAIT_V(2); PG8_BAR;
;         PG8_STAGE(PG8_SB(1, 0), cB + 128, boc); PG8_STAGE(PG8_SA(1, 0), cA + 128, aoc[0]); PG8_STAGE(PG8_SB(1, 1), cB + hB + 128, boc);
;         PG8_WAIT_V(6); PG8_BAR;
.LBB0_1230:
	s_sext_i32_i8 s6, s6
	s_lshl_b32 s71, s12, 8
	s_lshl_b32 s70, s6, 8
	s_add_u32 s12, s4, 0x2d300000
	s_addc_u32 s13, s5, 0
	s_add_u32 s14, s4, 0x1d300000
	s_addc_u32 s15, s5, 0
	s_lshl_b32 s4, s16, 5
	s_add_i32 s28, s20, 0x18000
	s_and_b32 s6, s4, 0x60
	s_add_i32 s60, s28, s19
	s_mov_b64 s[16:17], 0x80
	s_lshr_b32 s26, s6, 3
	s_lshl_b32 s27, s7, 13
	v_lshl_add_u64 v[8:9], v[8:9], 0, s[16:17]
	s_mov_b32 m0, s60
	s_add_i32 s61, s60, 0x2000
	s_add_i32 s62, s56, 0x8000
	s_add_i32 s63, s56, 0xa000
	s_waitcnt vmcnt(2)
	s_barrier
	global_load_lds_dwordx4 v[8:9], off
	v_lshl_add_u64 v[6:7], v[6:7], 0, s[16:17]
	s_mov_b32 m0, s61
	s_add_u32 s4, s44, 0x40080
	global_load_lds_dwordx4 v[6:7], off
	v_lshl_add_u64 v[2:3], v[2:3], 0, s[16:17]
	s_mov_b32 m0, s62
	s_addc_u32 s5, s45, 0
	s_add_i32 s29, s20, 0x1c000
	global_load_lds_dwordx4 v[2:3], off
	v_lshl_add_u64 v[2:3], v[4:5], 0, s[16:17]
	s_mov_b32 m0, s63
	s_add_i32 s64, s29, s19
	global_load_lds_dwordx4 v[2:3], off
	v_lshl_add_u64 v[2:3], s[4:5], 0, v[162:163]
	s_mov_b32 m0, s64
	s_add_i32 s65, s64, 0x2000
	global_load_lds_dwordx4 v[2:3], off
	v_lshl_add_u64 v[2:3], s[4:5], 0, v[166:167]
	s_mov_b32 m0, s65
	v_lshlrev_b32_e32 v6, 1, v10
	global_load_lds_dwordx4 v[2:3], off
	v_lshrrev_b32_e32 v2, 4, v10
	v_and_b32_e32 v3, 15, v10
	v_bfe_u32 v4, v10, 4, 2
	v_lshl_or_b32 v1, s7, 6, v3
	v_lshlrev_b32_e32 v3, 6, v3
	v_lshlrev_b32_e32 v5, 2, v10
	v_bfe_u32 v2, v2, 1, 1
	v_and_b32_e32 v6, 32, v6
	v_and_b32_e32 v5, 32, v5
	v_or_b32_e32 v7, v3, v6
	v_lshl_or_b32 v8, v2, 10, s27
	v_or_b32_e32 v2, s26, v2
	v_lshl_or_b32 v186, v4, 2, s6
	v_lshlrev_b32_e32 v4, 14, v15
	v_bitop3_b32 v3, v3, v5, v6 bitop3:0x36
	v_or_b32_e32 v6, 16, v7
	v_lshlrev_b32_e32 v2, 10, v2
	v_and_b32_e32 v4, 0xffff8000, v4
	v_bitop3_b32 v9, v7, v5, 16 bitop3:0x36
	v_bitop3_b32 v7, v2, v7, v5 bitop3:0xf6
	v_bitop3_b32 v2, v6, v2, v5 bitop3:0xde
	v_lshl_add_u32 v4, v16, 11, v4
	v_and_b32_e32 v5, 1, v15
	v_lshl_or_b32 v4, v5, 6, v4
	v_lshlrev_b32_sdwa v5, v13, sext(v17) dst_sel:DWORD dst_unused:UNUSED_PAD src0_sel:DWORD src1_sel:WORD_0
	v_add3_u32 v170, v4, v5, s23
	v_lshlrev_b32_e32 v4, 14, v11
	v_and_b32_e32 v4, 0xffff8000, v4
	s_waitcnt vmcnt(6)
	v_lshl_add_u32 v4, v12, 11, v4
	v_and_b32_e32 v5, 1, v11
	v_or_b32_e32 v3, v3, v8
	v_or_b32_e32 v8, v9, v8
	s_cmpk_lt_u32 s18, 0x100
	v_lshl_or_b32 v4, v5, 6, v4
	v_lshlrev_b32_sdwa v5, v13, sext(v14) dst_sel:DWORD dst_unused:UNUSED_PAD src0_sel:DWORD src1_sel:WORD_0
	v_mov_b32_e32 v165, v163
	v_mov_b32_e32 v169, v163
	s_cselect_b64 s[18:19], -1, 0
	s_ashr_i32 s66, s1, 31
	v_mov_b32_e32 v171, v163
	v_add3_u32 v172, v4, v5, s23
	v_mov_b32_e32 v173, v163
	s_mov_b32 s67, 0
	v_mov_b64_e32 v[174:175], 0x200
	v_mov_b64_e32 v[176:177], 0x1ff
	v_add_u32_e32 v187, s21, v7
	v_add_u32_e32 v188, s21, v2
	v_add_u32_e32 v189, s22, v7
	v_add_u32_e32 v190, s22, v2
	v_add_u32_e32 v191, s20, v3
	v_add_u32_e32 v192, s20, v8
	v_mov_b32_e32 v193, 0x79
	v_mov_b32_e32 v194, 0x7f
	v_add_u32_e32 v195, s28, v7
	v_add_u32_e32 v196, s28, v2
	v_add_u32_e32 v197, s29, v7
	v_add_u32_e32 v198, s29, v2
	v_mbcnt_lo_u32_b32 v255, -1, 0
	v_mbcnt_hi_u32_b32 v255, -1, v255
	v_and_b32_e32 v255, 16, v255
	v_xor_b32_e32 v187, v187, v255
	v_xor_b32_e32 v188, v188, v255
	v_xor_b32_e32 v189, v189, v255
	v_xor_b32_e32 v190, v190, v255
	v_xor_b32_e32 v191, v191, v255
	v_xor_b32_e32 v192, v192, v255
	v_xor_b32_e32 v195, v195, v255
	v_xor_b32_e32 v196, v196, v255
	v_xor_b32_e32 v197, v197, v255
	v_xor_b32_e32 v198, v198, v255
	s_mov_b64 s[20:21], 0x10000
	s_mov_b64 s[22:23], 0x20000
	s_mov_b64 s[26:27], 0x30000
	s_mov_b64 s[28:29], 0x80000
	s_mov_b64 s[30:31], 0x90000
	s_mov_b64 s[34:35], 0xa0000
	s_mov_b64 s[36:37], 0xb0000
	s_barrier
	s_branch .LBB0_1233

; #define GAS __attribute__((address_space(1)))
; #define PG8_STAGE(bufoff, gbase, voff) do { _Pragma("unroll") for (int _i = 0; _i < 2; ++_i) \
;         __builtin_amdgcn_global_load_lds((const GAS unsigned*)((const GAS char*)(gbase) + (voff)[_i]), (LAS unsigned*)(lds + (bufoff) + ldsw + _i * 8192), 16, 0, 0); } while (0)
; #define PG8_WAIT_V(n) asm volatile("s_waitcnt vmcnt(" #n ")" ::: "memory")
; #define PG8_BAR __builtin_amdgcn_s_barrier()
; #define PG8_OFFS(u, ao, bo) do { _Pragma("unroll") for (int _i = 0; _i < 2; ++_i) { (bo)[_i] = (unsigned)(sRb[_i] * (u).ldb + sC2[_i]); \
;         _Pragma("unroll") for (int _h = 0; _h < 2; ++_h) { int _r = _h * HALF + sR[_i]; if (GATHER) { _r = (u).gl ? (u).gl[_r] : ((_r < (u).gcnt) ? (u).gidx[_r] : 0); } (ao)[_h][_i] = (unsigned)(_r * (u).lda + sC2[_i]); } } } while (0)
; template <class Epi, class Sched, bool GATHER, bool FP8 = false, bool UNI = false>
; __device__ __forceinline__ void gemm_phase(LAS unsigned char* lds, const Sched& S, const Epi& E) {
;     ...
;     const int aoff = lds_byte(wr * 64 + fr, fq * 8), boff = lds_byte(wc * 32 + fr, fq * 8);
;     const int sclw = 0x79, scla = 0x7f;
;     const int aoff8[2] = {lds_byte(wr * 64 + fr, fq * 16), lds_byte(wr * 64 + fr, fq * 16 + 8)}, boff8[2] = {lds_byte(wc * 32 + fr, fq * 16), lds_byte(wc * 32 + fr, fq * 16 + 8)};
;     ...
;     Unit cur, nxt; int ui = 0;
;     if (!S.next(0, cur)) return;
;     f32x4 acc[2][2][4][2];
; #pragma unroll
;     for (int a = 0; a < 2; ++a)
; #pragma unroll
;         for (int b = 0; b < 2; ++b)
; #pragma unroll
;             for (int m = 0; m < 4; ++m)
; #pragma unroll
;                 for (int n = 0; n < 2; ++n) acc[a][b][m][n] = (f32x4){0.f, 0.f, 0.f, 0.f};
;     i32x8 At[4], B0[2], B1[2];
;     unsigned aoc[2][2], boc[2], aon[2][2], bon[2];
;     PG8_OFFS(cur, aoc, boc);
;     {
;         const GAS char* cA = cur.a; const GAS char* cB = cur.b; const size_t hB = (size_t)(Epi::WIDE ? 32 : HALF) * cur.ldb;
;         PG8_STAGE(PG8_SB(0, 0), cB, boc); PG8_STAGE(PG8_SB(0, 1), cB + hB, boc); PG8_STAGE(PG8_SA(0, 0), cA, aoc[0]); PG8_STAGE(PG8_SA(0, 1), cA, aoc[1]);
;         if (wr == 1) PG8_BAR;
;         PG8_WAIT_V(2); PG8_BAR;
;         PG8_STAGE(PG8_SB(1, 0), cB + 128, boc); PG8_STAGE(PG8_SA(1, 0), cA + 128, aoc[0]); PG8_STAGE(PG8_SB(1, 1), cB + hB + 128, boc);
;         PG8_WAIT_V(6); PG8_BAR;
.LBB0_1507:
	s_lshl_b32 s25, s25, 5
	v_lshrrev_b32_e32 v11, 4, v10
	v_and_b32_e32 v12, 15, v10
	s_and_b32 s45, s25, 0x60
	s_add_i32 s40, s97, s6
	v_lshl_or_b32 v175, s7, 6, v12
	s_lshr_b32 s25, s45, 3
	v_bfe_u32 v11, v11, 1, 1
	s_lshl_b32 s7, s7, 13
	v_lshl_add_u64 v[8:9], v[8:9], 0, s[66:67]
	s_mov_b32 m0, s40
	s_add_i32 s41, s40, 0x2000
	v_lshl_or_b32 v16, v11, 10, s7
	v_or_b32_e32 v11, s25, v11
	s_waitcnt vmcnt(2)
	s_barrier
	global_load_lds_dwordx4 v[8:9], off
	v_lshl_add_u64 v[6:7], v[6:7], 0, s[66:67]
	s_mov_b32 m0, s41
	s_add_i32 s49, s43, 0x8000
	s_add_i32 s25, s43, 0xa000
	global_load_lds_dwordx4 v[6:7], off
	v_lshl_add_u64 v[2:3], v[2:3], 0, s[66:67]
	s_mov_b32 m0, s49
	s_add_u32 s38, s78, 0x40080
	global_load_lds_dwordx4 v[2:3], off
	v_lshl_add_u64 v[2:3], v[4:5], 0, s[66:67]
	s_mov_b32 m0, s25
	s_addc_u32 s39, s79, 0
	s_add_i32 s61, s58, s6
	global_load_lds_dwordx4 v[2:3], off
	v_lshl_add_u64 v[2:3], s[38:39], 0, v[172:173]
	s_mov_b32 m0, s61
	s_add_i32 s50, s61, 0x2000
	global_load_lds_dwordx4 v[2:3], off
	v_lshl_add_u64 v[2:3], s[38:39], 0, v[170:171]
	s_mov_b32 m0, s50
	v_bfe_u32 v13, v10, 4, 2
	global_load_lds_dwordx4 v[2:3], off
	v_lshlrev_b32_e32 v14, 2, v10
	v_lshlrev_b32_e32 v10, 1, v10
	v_lshlrev_b32_e32 v12, 6, v12
	v_and_b32_e32 v10, 32, v10
	v_and_b32_e32 v14, 32, v14
	v_or_b32_e32 v15, v12, v10
	v_bitop3_b32 v10, v12, v14, v10 bitop3:0x36
	v_bitop3_b32 v17, v15, v14, 16 bitop3:0x36
	s_waitcnt vmcnt(6)
	v_or_b32_e32 v10, v10, v16
	v_or_b32_e32 v12, 16, v15
	v_or_b32_e32 v16, v17, v16
	v_lshlrev_b32_e32 v11, 10, v11
	s_cmpk_lt_u32 s13, 0x100
	v_mov_b32_e32 v34, 0
	v_bitop3_b32 v179, v11, v15, v14 bitop3:0xf6
	v_bitop3_b32 v203, v12, v11, v14 bitop3:0xde
	s_cselect_b64 s[74:75], -1, 0
	v_lshl_or_b32 v204, v13, 3, s45
	v_ashrrev_i32_e32 v167, 31, v166
	v_ashrrev_i32_e32 v169, 31, v168
	s_mov_b32 s38, 0
	v_add_u32_e32 v205, s0, v10
	v_add_u32_e32 v206, s0, v16
	v_mbcnt_lo_u32_b32 v255, -1, 0
	v_mbcnt_hi_u32_b32 v255, -1, v255
	v_and_b32_e32 v255, 16, v255
	v_xor_b32_e32 v179, v179, v255
	v_xor_b32_e32 v203, v203, v255
	v_xor_b32_e32 v205, v205, v255
	v_xor_b32_e32 v206, v206, v255
	v_mov_b32_e32 v35, v34
	v_mov_b32_e32 v36, v34
	v_mov_b32_e32 v37, v34
	v_mov_b32_e32 v38, v34
	v_mov_b32_e32 v39, v34
	v_mov_b32_e32 v40, v34
	v_mov_b32_e32 v41, v34
	v_mov_b32_e32 v42, v34
	v_mov_b32_e32 v43, v34
	v_mov_b32_e32 v44, v34
	v_mov_b32_e32 v45, v34
	v_mov_b32_e32 v46, v34
	v_mov_b32_e32 v47, v34
	v_mov_b32_e32 v48, v34
	v_mov_b32_e32 v49, v34
	v_mov_b32_e32 v50, v34
	v_mov_b32_e32 v51, v34
	v_mov_b32_e32 v52, v34
	v_mov_b32_e32 v53, v34
	v_mov_b32_e32 v54, v34
	v_mov_b32_e32 v55, v34
	v_mov_b32_e32 v56, v34
	v_mov_b32_e32 v57, v34
	v_mov_b32_e32 v58, v34
	v_mov_b32_e32 v59, v34
	v_mov_b32_e32 v60, v34
	v_mov_b32_e32 v61, v34
	v_mov_b32_e32 v62, v34
	v_mov_b32_e32 v63, v34
	v_mov_b32_e32 v64, v34
	v_mov_b32_e32 v65, v34
	v_mov_b32_e32 v66, v34
	v_mov_b32_e32 v67, v34
	v_mov_b32_e32 v68, v34
	v_mov_b32_e32 v69, v34
	v_mov_b32_e32 v70, v34
	v_mov_b32_e32 v71, v34
	v_mov_b32_e32 v72, v34
	v_mov_b32_e32 v73, v34
	v_mov_b32_e32 v74, v34
	v_mov_b32_e32 v75, v34
	v_mov_b32_e32 v76, v34
	v_mov_b32_e32 v77, v34
	v_mov_b32_e32 v78, v34
	v_mov_b32_e32 v79, v34
	v_mov_b32_e32 v80, v34
	v_mov_b32_e32 v81, v34
	v_mov_b32_e32 v82, v34
	v_mov_b32_e32 v83, v34
	v_mov_b32_e32 v84, v34
	v_mov_b32_e32 v85, v34
	v_mov_b32_e32 v86, v34
	v_mov_b32_e32 v87, v34
	v_mov_b32_e32 v88, v34
	v_mov_b32_e32 v89, v34
	v_mov_b32_e32 v90, v34
	v_mov_b32_e32 v91, v34
	v_mov_b32_e32 v92, v34
	v_mov_b32_e32 v93, v34
	v_mov_b32_e32 v94, v34
	v_mov_b32_e32 v95, v34
	v_mov_b32_e32 v96, v34
	v_mov_b32_e32 v97, v34
	v_mov_b32_e32 v98, v34
	v_mov_b32_e32 v99, v34
	v_mov_b32_e32 v100, v34
	v_mov_b32_e32 v101, v34
	v_mov_b32_e32 v102, v34
	v_mov_b32_e32 v103, v34
	v_mov_b32_e32 v104, v34
	v_mov_b32_e32 v105, v34
	v_mov_b32_e32 v106, v34
	v_mov_b32_e32 v107, v34
	v_mov_b32_e32 v108, v34
	v_mov_b32_e32 v109, v34
	v_mov_b32_e32 v110, v34
	v_mov_b32_e32 v111, v34
	v_mov_b32_e32 v112, v34
	v_mov_b32_e32 v113, v34
	v_mov_b32_e32 v114, v34
	v_mov_b32_e32 v115, v34
	v_mov_b32_e32 v116, v34
	v_mov_b32_e32 v117, v34
	v_mov_b32_e32 v118, v34
	v_mov_b32_e32 v119, v34
	v_mov_b32_e32 v120, v34
	v_mov_b32_e32 v121, v34
	v_mov_b32_e32 v122, v34
	v_mov_b32_e32 v123, v34
	v_mov_b32_e32 v124, v34
	v_mov_b32_e32 v125, v34
	v_mov_b32_e32 v126, v34
	v_mov_b32_e32 v127, v34
	v_mov_b32_e32 v128, v34
	v_mov_b32_e32 v129, v34
	v_mov_b32_e32 v130, v34
	v_mov_b32_e32 v131, v34
	v_mov_b32_e32 v132, v34
	v_mov_b32_e32 v133, v34
	v_mov_b32_e32 v134, v34
	v_mov_b32_e32 v135, v34
	v_mov_b32_e32 v136, v34
	v_mov_b32_e32 v137, v34
	v_mov_b32_e32 v138, v34
	v_mov_b32_e32 v139, v34
	v_mov_b32_e32 v140, v34
	v_mov_b32_e32 v141, v34
	v_mov_b32_e32 v142, v34
	v_mov_b32_e32 v143, v34
	v_mov_b32_e32 v144, v34
	v_mov_b32_e32 v145, v34
	v_mov_b32_e32 v146, v34
	v_mov_b32_e32 v147, v34
	v_mov_b32_e32 v148, v34
	v_mov_b32_e32 v149, v34
	v_mov_b32_e32 v150, v34
	v_mov_b32_e32 v151, v34
	v_mov_b32_e32 v152, v34
	v_mov_b32_e32 v153, v34
	v_mov_b32_e32 v154, v34
	v_mov_b32_e32 v155, v34
	v_mov_b32_e32 v156, v34
	v_mov_b32_e32 v157, v34
	v_mov_b32_e32 v158, v34
	v_mov_b32_e32 v159, v34
	v_mov_b32_e32 v160, v34
	v_mov_b32_e32 v161, v34
	s_barrier
	s_branch .LBB0_1510

; #define GAS __attribute__((address_space(1)))
; #define PG8_STAGE(bufoff, gbase, voff) do { _Pragma("unroll") for (int _i = 0; _i < 2; ++_i) \
;         __builtin_amdgcn_global_load_lds((const GAS unsigned*)((const GAS char*)(gbase) + (voff)[_i]), (LAS unsigned*)(lds + (bufoff) + ldsw + _i * 8192), 16, 0, 0); } while (0)
; #define PG8_WAIT_V(n) asm volatile("s_waitcnt vmcnt(" #n ")" ::: "memory")
; #define PG8_BAR __builtin_amdgcn_s_barrier()
; #define PG8_OFFS(u, ao, bo) do { _Pragma("unroll") for (int _i = 0; _i < 2; ++_i) { (bo)[_i] = (unsigned)(sRb[_i] * (u).ldb + sC2[_i]); \
;         _Pragma("unroll") for (int _h = 0; _h < 2; ++_h) { int _r = _h * HALF + sR[_i]; if (GATHER) { _r = (u).gl ? (u).gl[_r] : ((_r < (u).gcnt) ? (u).gidx[_r] : 0); } (ao)[_h][_i] = (unsigned)(_r * (u).lda + sC2[_i]); } } } while (0)
; template <class Epi, class Sched, bool GATHER, bool FP8 = false, bool UNI = false>
; __device__ __forceinline__ void gemm_phase(LAS unsigned char* lds, const Sched& S, const Epi& E) {
;     ...
;     const int aoff = lds_byte(wr * 64 + fr, fq * 8), boff = lds_byte(wc * 32 + fr, fq * 8);
;     const int sclw = 0x79, scla = 0x7f;
;     const int aoff8[2] = {lds_byte(wr * 64 + fr, fq * 16), lds_byte(wr * 64 + fr, fq * 16 + 8)}, boff8[2] = {lds_byte(wc * 32 + fr, fq * 16), lds_byte(wc * 32 + fr, fq * 16 + 8)};
;     ...
;     Unit cur, nxt; int ui = 0;
;     if (!S.next(0, cur)) return;
;     f32x4 acc[2][2][4][2];
; #pragma unroll
;     for (int a = 0; a < 2; ++a)
; #pragma unroll
;         for (int b = 0; b < 2; ++b)
; #pragma unroll
;             for (int m = 0; m < 4; ++m)
; #pragma unroll
;                 for (int n = 0; n < 2; ++n) acc[a][b][m][n] = (f32x4){0.f, 0.f, 0.f, 0.f};
;     i32x8 At[4], B0[2], B1[2];
;     unsigned aoc[2][2], boc[2], aon[2][2], bon[2];
;     PG8_OFFS(cur, aoc, boc);
;     {
;         const GAS char* cA = cur.a; const GAS char* cB = cur.b; const size_t hB = (size_t)(Epi::WIDE ? 32 : HALF) * cur.ldb;
;         PG8_STAGE(PG8_SB(0, 0), cB, boc); PG8_STAGE(PG8_SB(0, 1), cB + hB, boc); PG8_STAGE(PG8_SA(0, 0), cA, aoc[0]); PG8_STAGE(PG8_SA(0, 1), cA, aoc[1]);
;         if (wr == 1) PG8_BAR;
;         PG8_WAIT_V(2); PG8_BAR;
;         PG8_STAGE(PG8_SB(1, 0), cB + 128, boc); PG8_STAGE(PG8_SA(1, 0), cA + 128, aoc[0]); PG8_STAGE(PG8_SB(1, 1), cB + hB + 128, boc);
;         PG8_WAIT_V(6); PG8_BAR;
.LBB0_1944:
	s_lshl_b32 s68, s12, 8
	s_lshl_b32 s69, s10, 8
	s_and_b32 s29, s15, 3
	s_lshl_b32 s49, s19, 6
	s_add_u32 s8, s8, 0x3fb00000
	s_addc_u32 s9, s9, 0
	s_add_i32 s30, s16, 0x18000
	s_add_i32 s50, s30, s26
	s_mov_b64 s[10:11], 0x80
	v_lshl_add_u64 v[8:9], v[8:9], 0, s[10:11]
	s_mov_b32 m0, s50
	s_add_i32 s51, s50, 0x2000
	s_add_i32 s56, s45, 0x8000
	s_add_i32 s57, s45, 0xa000
	s_waitcnt vmcnt(2)
	s_barrier
	global_load_lds_dwordx4 v[8:9], off
	v_lshl_add_u64 v[6:7], v[6:7], 0, s[10:11]
	s_mov_b32 m0, s51
	s_add_u32 s12, s22, 0x4080
	global_load_lds_dwordx4 v[6:7], off
	v_lshl_add_u64 v[2:3], v[2:3], 0, s[10:11]
	s_mov_b32 m0, s56
	s_addc_u32 s13, s23, 0
	s_add_i32 s31, s16, 0x1c000
	global_load_lds_dwordx4 v[2:3], off
	v_lshl_add_u64 v[2:3], v[4:5], 0, s[10:11]
	s_mov_b32 m0, s57
	s_add_i32 s58, s31, s26
	global_load_lds_dwordx4 v[2:3], off
	v_lshl_add_u64 v[2:3], s[12:13], 0, v[162:163]
	s_mov_b32 m0, s58
	s_add_i32 s59, s58, 0x2000
	global_load_lds_dwordx4 v[2:3], off
	v_lshl_add_u64 v[2:3], s[12:13], 0, v[168:169]
	s_mov_b32 m0, s59
	v_lshlrev_b32_e32 v5, 1, v1
	global_load_lds_dwordx4 v[2:3], off
	v_lshlrev_b32_e32 v3, 6, v1
	s_cmpk_lt_u32 s14, 0x100
	v_and_b32_e32 v3, 0x3c0, v3
	v_lshlrev_b32_e32 v4, 2, v1
	v_and_b32_e32 v5, 32, v5
	v_lshlrev_b32_e32 v7, 5, v1
	s_cselect_b64 s[12:13], -1, 0
	s_lshl_b32 s14, s15, 11
	v_and_b32_e32 v4, 32, v4
	v_or_b32_e32 v6, v3, v5
	v_and_b32_e32 v7, 0x400, v7
	s_add_i32 s14, s16, s14
	v_lshrrev_b32_e32 v2, 1, v1
	v_lshl_or_b32 v8, s19, 13, v7
	v_bitop3_b32 v5, v3, v4, v5 bitop3:0x36
	v_bitop3_b32 v4, v6, v4, 16 bitop3:0x36
	v_lshl_or_b32 v7, s29, 12, v7
	s_waitcnt vmcnt(6)
	s_add_i32 s14, s14, 0x20000
	s_lshl_b32 s60, s29, 6
	v_bfe_u32 v174, v1, 2, 4
	s_add_i32 s61, s16, 0x24104
	s_ashr_i32 s62, s18, 3
	s_and_b32 s63, s17, 7
	s_ashr_i32 s64, s17, 3
	v_and_b32_e32 v2, 24, v2
	v_or_b32_e32 v9, v5, v8
	v_or_b32_e32 v6, v4, v8
	v_or_b32_e32 v5, v5, v7
	v_or_b32_e32 v4, v4, v7
	v_and_b32_e32 v176, 48, v10
	v_add_u32_e32 v3, s14, v3
	v_lshl_add_u32 v7, v174, 6, s14
	s_cmp_lt_i32 s64, s62
	v_mov_b32_e32 v167, v163
	v_mov_b32_e32 v173, v163
	v_mov_b32_e32 v175, v163
	v_mov_b32_e32 v177, v163
	s_mov_b32 s65, 0
	s_cselect_b64 s[14:15], -1, 0
	v_add_u32_e32 v1, s27, v5
	v_add_u32_e32 v186, s27, v4
	v_add_u32_e32 v187, s28, v5
	v_add_u32_e32 v188, s28, v4
	v_add_u32_e32 v189, s16, v9
	v_add_u32_e32 v190, s16, v6
	v_mov_b32_e32 v191, 0x79
	v_mov_b32_e32 v192, 0x7f
	v_add_u32_e32 v193, s30, v5
	v_add_u32_e32 v194, s30, v4
	v_add_u32_e32 v195, s31, v5
	v_add_u32_e32 v196, s31, v4
	v_mbcnt_lo_u32_b32 v255, -1, 0
	v_mbcnt_hi_u32_b32 v255, -1, v255
	v_and_b32_e32 v255, 16, v255
	v_xor_b32_e32 v1, v1, v255
	v_xor_b32_e32 v186, v186, v255
	v_xor_b32_e32 v187, v187, v255
	v_xor_b32_e32 v188, v188, v255
	v_xor_b32_e32 v189, v189, v255
	v_xor_b32_e32 v190, v190, v255
	v_xor_b32_e32 v193, v193, v255
	v_xor_b32_e32 v194, v194, v255
	v_xor_b32_e32 v195, v195, v255
	v_xor_b32_e32 v196, v196, v255
	v_add_u32_e32 v197, v3, v2
	v_add_u32_e32 v198, v7, v176
	s_barrier
	s_waitcnt vmcnt(0)
	s_branch .LBB0_1947

; #define GAS __attribute__((address_space(1)))
; #define PG8_STAGE(bufoff, gbase, voff) do { _Pragma("unroll") for (int _i = 0; _i < 2; ++_i) \
;         __builtin_amdgcn_global_load_lds((const GAS unsigned*)((const GAS char*)(gbase) + (voff)[_i]), (LAS unsigned*)(lds + (bufoff) + ldsw + _i * 8192), 16, 0, 0); } while (0)
; #define PG8_WAIT_V(n) asm volatile("s_waitcnt vmcnt(" #n ")" ::: "memory")
; #define PG8_BAR __builtin_amdgcn_s_barrier()
; #define PG8_OFFS(u, ao, bo) do { _Pragma("unroll") for (int _i = 0; _i < 2; ++_i) { (bo)[_i] = (unsigned)(sRb[_i] * (u).ldb + sC2[_i]); \
;         _Pragma("unroll") for (int _h = 0; _h < 2; ++_h) { int _r = _h * HALF + sR[_i]; if (GATHER) { _r = (u).gl ? (u).gl[_r] : ((_r < (u).gcnt) ? (u).gidx[_r] : 0); } (ao)[_h][_i] = (unsigned)(_r * (u).lda + sC2[_i]); } } } while (0)
; template <class Epi, class Sched, bool GATHER, bool FP8 = false, bool UNI = false>
; __device__ __forceinline__ void gemm_phase(LAS unsigned char* lds, const Sched& S, const Epi& E) {
;     ...
;     const int aoff = lds_byte(wr * 64 + fr, fq * 8), boff = lds_byte(wc * 32 + fr, fq * 8);
;     const int sclw = 0x79, scla = 0x7f;
;     const int aoff8[2] = {lds_byte(wr * 64 + fr, fq * 16), lds_byte(wr * 64 + fr, fq * 16 + 8)}, boff8[2] = {lds_byte(wc * 32 + fr, fq * 16), lds_byte(wc * 32 + fr, fq * 16 + 8)};
;     ...
;     Unit cur, nxt; int ui = 0;
;     if (!S.next(0, cur)) return;
;     f32x4 acc[2][2][4][2];
; #pragma unroll
;     for (int a = 0; a < 2; ++a)
; #pragma unroll
;         for (int b = 0; b < 2; ++b)
; #pragma unroll
;             for (int m = 0; m < 4; ++m)
; #pragma unroll
;                 for (int n = 0; n < 2; ++n) acc[a][b][m][n] = (f32x4){0.f, 0.f, 0.f, 0.f};
;     i32x8 At[4], B0[2], B1[2];
;     unsigned aoc[2][2], boc[2], aon[2][2], bon[2];
;     PG8_OFFS(cur, aoc, boc);
;     {
;         const GAS char* cA = cur.a; const GAS char* cB = cur.b; const size_t hB = (size_t)(Epi::WIDE ? 32 : HALF) * cur.ldb;
;         PG8_STAGE(PG8_SB(0, 0), cB, boc); PG8_STAGE(PG8_SB(0, 1), cB + hB, boc); PG8_STAGE(PG8_SA(0, 0), cA, aoc[0]); PG8_STAGE(PG8_SA(0, 1), cA, aoc[1]);
;         if (wr == 1) PG8_BAR;
;         PG8_WAIT_V(2); PG8_BAR;
;         PG8_STAGE(PG8_SB(1, 0), cB + 128, boc); PG8_STAGE(PG8_SA(1, 0), cA + 128, aoc[0]); PG8_STAGE(PG8_SB(1, 1), cB + hB + 128, boc);
;         PG8_WAIT_V(6); PG8_BAR;
.LBB0_2174:
	s_add_i32 s27, s0, 0x18000
	s_add_i32 s61, s27, s22
	s_mov_b64 s[20:21], 0x80
	s_and_b32 s7, s7, 3
	v_lshl_add_u64 v[8:9], v[8:9], 0, s[20:21]
	s_mov_b32 m0, s61
	s_add_i32 s68, s61, 0x2000
	s_add_i32 s69, s56, 0x8000
	s_add_i32 s70, s56, 0xa000
	s_waitcnt vmcnt(2)
	s_barrier
	global_load_lds_dwordx4 v[8:9], off
	v_lshl_add_u64 v[6:7], v[6:7], 0, s[20:21]
	s_mov_b32 m0, s68
	s_add_u32 s28, s42, 0x40080
	global_load_lds_dwordx4 v[6:7], off
	v_lshl_add_u64 v[2:3], v[2:3], 0, s[20:21]
	s_mov_b32 m0, s69
	s_addc_u32 s29, s43, 0
	s_add_i32 s30, s0, 0x1c000
	global_load_lds_dwordx4 v[2:3], off
	v_lshl_add_u64 v[2:3], v[4:5], 0, s[20:21]
	s_mov_b32 m0, s70
	s_add_i32 s71, s30, s22
	global_load_lds_dwordx4 v[2:3], off
	v_lshl_add_u64 v[2:3], s[28:29], 0, v[162:163]
	s_mov_b32 m0, s71
	s_add_i32 s72, s71, 0x2000
	global_load_lds_dwordx4 v[2:3], off
	v_lshl_add_u64 v[2:3], s[28:29], 0, v[168:169]
	s_mov_b32 m0, s72
	v_bfe_u32 v18, v10, 4, 2
	global_load_lds_dwordx4 v[2:3], off
	v_and_b32_e32 v17, 15, v10
	v_lshlrev_b32_e32 v19, 3, v18
	v_lshlrev_b32_e32 v18, 5, v18
	v_lshl_or_b32 v1, s17, 6, v17
	v_lshlrev_b32_e32 v17, 6, v17
	v_lshlrev_b32_e32 v20, 2, v10
	v_and_b32_e32 v21, 32, v18
	v_lshlrev_b32_e32 v2, 5, v10
	v_and_b32_e32 v20, 32, v20
	v_or_b32_e32 v22, v17, v21
	v_and_b32_e32 v2, 0x400, v2
	v_lshl_or_b32 v3, s17, 13, v2
	v_bitop3_b32 v4, v17, v20, v21 bitop3:0x36
	v_bitop3_b32 v6, v22, v20, 16 bitop3:0x36
	v_lshl_or_b32 v2, s7, 12, v2
	v_or_b32_e32 v5, v4, v3
	v_or_b32_e32 v3, v6, v3
	v_or_b32_e32 v4, v4, v2
	v_or_b32_e32 v2, v6, v2
	v_lshlrev_b32_e32 v6, 14, v14
	v_and_b32_e32 v6, 0xffff8000, v6
	v_lshl_add_u32 v6, v15, 11, v6
	v_and_b32_e32 v7, 1, v14
	v_lshl_or_b32 v6, v7, 6, v6
	v_lshlrev_b32_e32 v7, 1, v16
	v_add3_u32 v182, v6, v7, s26
	v_lshlrev_b32_e32 v6, 14, v11
	v_and_b32_e32 v6, 0xffff8000, v6
	s_waitcnt vmcnt(6)
	v_lshl_or_b32 v176, s7, 5, v19
	v_lshl_or_b32 v174, s7, 7, v18
	v_lshl_add_u32 v6, v12, 11, v6
	v_and_b32_e32 v7, 1, v11
	s_cmpk_lt_u32 s6, 0x100
	v_lshl_add_u64 v[178:179], s[14:15], 0, v[174:175]
	v_lshlrev_b32_e32 v174, 2, v176
	v_lshl_or_b32 v6, v7, 6, v6
	v_lshlrev_b32_e32 v7, 1, v13
	s_mov_b32 s17, 0
	v_mov_b32_e32 v167, v175
	v_mov_b32_e32 v173, v175
	s_cselect_b64 s[22:23], -1, 0
	s_ashr_i32 s73, s3, 31
	v_lshl_add_u64 v[180:181], s[12:13], 0, v[174:175]
	v_mov_b32_e32 v183, v175
	v_add3_u32 v184, v6, v7, s26
	v_mov_b32_e32 v185, v175
	v_mov_b64_e32 v[186:187], 0xb80
	v_mov_b64_e32 v[188:189], 0xb7f
	s_movk_i32 s74, 0x171
	v_add_u32_e32 v177, s4, v4
	v_add_u32_e32 v198, s4, v2
	v_add_u32_e32 v199, s5, v4
	v_add_u32_e32 v200, s5, v2
	v_add_u32_e32 v201, s0, v5
	v_add_u32_e32 v202, s0, v3
	v_mov_b32_e32 v203, 0x79
	v_mov_b32_e32 v204, 0x7f
	v_add_u32_e32 v205, s27, v4
	v_add_u32_e32 v206, s27, v2
	v_add_u32_e32 v207, s30, v4
	v_add_u32_e32 v208, s30, v2
	v_mbcnt_lo_u32_b32 v255, -1, 0
	v_mbcnt_hi_u32_b32 v255, -1, v255
	v_and_b32_e32 v255, 16, v255
	v_xor_b32_e32 v177, v177, v255
	v_xor_b32_e32 v198, v198, v255
	v_xor_b32_e32 v199, v199, v255
	v_xor_b32_e32 v200, v200, v255
	v_xor_b32_e32 v201, v201, v255
	v_xor_b32_e32 v202, v202, v255
	v_xor_b32_e32 v205, v205, v255
	v_xor_b32_e32 v206, v206, v255
	v_xor_b32_e32 v207, v207, v255
	v_xor_b32_e32 v208, v208, v255
	s_mov_b32 s0, 0x800000
	s_mov_b32 s75, 0x3f317217
	s_mov_b32 s76, 0x7f800000
	s_mov_b32 s77, 0x400000
	s_mov_b32 s78, 0x401000
	s_movk_i32 s79, 0x3000
	s_mov_b32 s80, 0x403000
	s_mov_b32 s81, 0x9000
	s_mov_b32 s82, 0x409000
	s_mov_b32 s83, 0x40a000
	s_mov_b32 s84, 0xb000
	s_mov_b64 s[12:13], 0x1000
	s_mov_b64 s[14:15], 0x2000
	s_mov_b64 s[26:27], 0x3000
	s_mov_b64 s[28:29], 0x8000
	s_mov_b64 s[30:31], 0x9000
	s_mov_b64 s[34:35], 0xa000
	s_mov_b64 s[36:37], 0xb000
	v_mov_b32_e32 v209, 0x41b17218
	s_mov_b32 s85, s17
	s_barrier
	s_branch .LBB0_2177

; #define GAS __attribute__((address_space(1)))
; #define PG8_STAGE(bufoff, gbase, voff) do { _Pragma("unroll") for (int _i = 0; _i < 2; ++_i) \
;         __builtin_amdgcn_global_load_lds((const GAS unsigned*)((const GAS char*)(gbase) + (voff)[_i]), (LAS unsigned*)(lds + (bufoff) + ldsw + _i * 8192), 16, 0, 0); } while (0)
; #define PG8_WAIT_V(n) asm volatile("s_waitcnt vmcnt(" #n ")" ::: "memory")
; #define PG8_BAR __builtin_amdgcn_s_barrier()
; #define PG8_OFFS(u, ao, bo) do { _Pragma("unroll") for (int _i = 0; _i < 2; ++_i) { (bo)[_i] = (unsigned)(sRb[_i] * (u).ldb + sC2[_i]); \
;         _Pragma("unroll") for (int _h = 0; _h < 2; ++_h) { int _r = _h * HALF + sR[_i]; if (GATHER) { _r = (u).gl ? (u).gl[_r] : ((_r < (u).gcnt) ? (u).gidx[_r] : 0); } (ao)[_h][_i] = (unsigned)(_r * (u).lda + sC2[_i]); } } } while (0)
; template <class Epi, class Sched, bool GATHER, bool FP8 = false, bool UNI = false>
; __device__ __forceinline__ void gemm_phase(LAS unsigned char* lds, const Sched& S, const Epi& E) {
;     ...
;     const int aoff = lds_byte(wr * 64 + fr, fq * 8), boff = lds_byte(wc * 32 + fr, fq * 8);
;     const int sclw = 0x79, scla = 0x7f;
;     const int aoff8[2] = {lds_byte(wr * 64 + fr, fq * 16), lds_byte(wr * 64 + fr, fq * 16 + 8)}, boff8[2] = {lds_byte(wc * 32 + fr, fq * 16), lds_byte(wc * 32 + fr, fq * 16 + 8)};
;     ...
;     Unit cur, nxt; int ui = 0;
;     if (!S.next(0, cur)) return;
;     f32x4 acc[2][2][4][2];
; #pragma unroll
;     for (int a = 0; a < 2; ++a)
; #pragma unroll
;         for (int b = 0; b < 2; ++b)
; #pragma unroll
;             for (int m = 0; m < 4; ++m)
; #pragma unroll
;                 for (int n = 0; n < 2; ++n) acc[a][b][m][n] = (f32x4){0.f, 0.f, 0.f, 0.f};
;     i32x8 At[4], B0[2], B1[2];
;     unsigned aoc[2][2], boc[2], aon[2][2], bon[2];
;     PG8_OFFS(cur, aoc, boc);
;     {
;         const GAS char* cA = cur.a; const GAS char* cB = cur.b; const size_t hB = (size_t)(Epi::WIDE ? 32 : HALF) * cur.ldb;
;         PG8_STAGE(PG8_SB(0, 0), cB, boc); PG8_STAGE(PG8_SB(0, 1), cB + hB, boc); PG8_STAGE(PG8_SA(0, 0), cA, aoc[0]); PG8_STAGE(PG8_SA(0, 1), cA, aoc[1]);
;         if (wr == 1) PG8_BAR;
;         PG8_WAIT_V(2); PG8_BAR;
;         PG8_STAGE(PG8_SB(1, 0), cB + 128, boc); PG8_STAGE(PG8_SA(1, 0), cA + 128, aoc[0]); PG8_STAGE(PG8_SB(1, 1), cB + hB + 128, boc);
;         PG8_WAIT_V(6); PG8_BAR;
.LBB0_3049:
	s_add_u32 s20, s6, 0x35b00000
	s_addc_u32 s21, s7, 0
	s_lshl_b32 s22, s22, 5
	v_lshrrev_b32_e32 v11, 4, v10
	v_and_b32_e32 v12, 15, v10
	s_and_b32 s35, s22, 0x60
	v_lshl_or_b32 v193, s5, 6, v12
	s_lshr_b32 s22, s35, 3
	v_bfe_u32 v11, v11, 1, 1
	s_lshl_b32 s5, s5, 13
	s_add_i32 s67, s34, 0x18000
	v_lshl_or_b32 v16, v11, 10, s5
	v_or_b32_e32 v11, s22, v11
	s_add_i32 s68, s67, s4
	s_mov_b64 s[22:23], 0x80
	v_lshl_add_u64 v[8:9], v[8:9], 0, s[22:23]
	s_mov_b32 m0, s68
	s_add_i32 s69, s68, 0x2000
	s_add_i32 s70, s59, 0x8000
	s_add_i32 s71, s59, 0xa000
	s_waitcnt vmcnt(2)
	s_barrier
	global_load_lds_dwordx4 v[8:9], off
	v_lshl_add_u64 v[4:5], v[4:5], 0, s[22:23]
	s_mov_b32 m0, s69
	s_add_u32 s30, s40, 0x40080
	global_load_lds_dwordx4 v[4:5], off
	v_lshl_add_u64 v[4:5], v[6:7], 0, s[22:23]
	s_mov_b32 m0, s70
	s_addc_u32 s31, s41, 0
	s_add_i32 s72, s34, 0x1c000
	global_load_lds_dwordx4 v[4:5], off
	v_lshl_add_u64 v[2:3], v[2:3], 0, s[22:23]
	s_mov_b32 m0, s71
	s_add_i32 s73, s72, s4
	global_load_lds_dwordx4 v[2:3], off
	v_lshl_add_u64 v[2:3], s[30:31], 0, v[168:169]
	s_mov_b32 m0, s73
	s_add_i32 s74, s73, 0x2000
	global_load_lds_dwordx4 v[2:3], off
	v_lshl_add_u64 v[2:3], s[30:31], 0, v[166:167]
	s_mov_b32 m0, s74
	v_bfe_u32 v13, v10, 4, 2
	global_load_lds_dwordx4 v[2:3], off
	v_lshlrev_b32_e32 v14, 2, v10
	v_lshlrev_b32_e32 v10, 1, v10
	v_lshlrev_b32_e32 v12, 6, v12
	v_and_b32_e32 v10, 32, v10
	s_cmpk_lt_u32 s26, 0x100
	v_and_b32_e32 v14, 32, v14
	v_or_b32_e32 v15, v12, v10
	s_cselect_b64 s[26:27], -1, 0
	s_add_i32 s75, s34, 0x24104
	s_ashr_i32 s76, s29, 3
	s_and_b32 s77, s28, 7
	s_ashr_i32 s78, s28, 3
	v_bitop3_b32 v10, v12, v14, v10 bitop3:0x36
	v_bitop3_b32 v17, v15, v14, 16 bitop3:0x36
	s_waitcnt vmcnt(6)
	s_cmp_lt_i32 s78, s76
	v_or_b32_e32 v10, v10, v16
	v_or_b32_e32 v12, 16, v15
	v_or_b32_e32 v16, v17, v16
	v_lshlrev_b32_e32 v11, 10, v11
	s_cselect_b64 s[28:29], -1, 0
	s_add_u32 s79, s6, 0x35a00000
	v_add_u32_e32 v173, 0x80, v164
	v_add_u32_e32 v177, 0x80, v162
	v_bitop3_b32 v194, v11, v15, v14 bitop3:0xf6
	v_bitop3_b32 v195, v12, v11, v14 bitop3:0xde
	v_lshl_or_b32 v196, v13, 3, s35
	v_ashrrev_i32_e32 v163, 31, v162
	v_ashrrev_i32_e32 v165, 31, v164
	s_addc_u32 s80, s7, 0
	s_mov_b32 s83, 0
	s_mov_b64 s[30:31], 0
	v_mov_b32_e32 v201, 0x100
	v_add_u32_e32 v197, s34, v10
	v_add_u32_e32 v198, s34, v16
	v_mbcnt_lo_u32_b32 v255, -1, 0
	v_mbcnt_hi_u32_b32 v255, -1, v255
	v_and_b32_e32 v255, 16, v255
	v_xor_b32_e32 v194, v194, v255
	v_xor_b32_e32 v195, v195, v255
	v_xor_b32_e32 v197, v197, v255
	v_xor_b32_e32 v198, v198, v255
	v_mov_b32_e32 v199, 0x79
	v_mov_b32_e32 v200, 0x7f
	s_mov_b32 s81, 0x12000
	v_mov_b32_e32 v34, v171
	v_mov_b32_e32 v35, v171
	v_mov_b32_e32 v36, v171
	v_mov_b32_e32 v37, v171
	v_mov_b32_e32 v38, v171
	v_mov_b32_e32 v39, v171
	v_mov_b32_e32 v40, v171
	v_mov_b32_e32 v41, v171
	v_mov_b32_e32 v42, v171
	v_mov_b32_e32 v43, v171
	v_mov_b32_e32 v44, v171
	v_mov_b32_e32 v45, v171
	v_mov_b32_e32 v46, v171
	v_mov_b32_e32 v47, v171
	v_mov_b32_e32 v48, v171
	v_mov_b32_e32 v49, v171
	v_mov_b32_e32 v50, v171
	v_mov_b32_e32 v51, v171
	v_mov_b32_e32 v52, v171
	v_mov_b32_e32 v53, v171
	v_mov_b32_e32 v54, v171
	v_mov_b32_e32 v55, v171
	v_mov_b32_e32 v56, v171
	v_mov_b32_e32 v57, v171
	v_mov_b32_e32 v58, v171
	v_mov_b32_e32 v59, v171
	v_mov_b32_e32 v60, v171
	v_mov_b32_e32 v61, v171
	v_mov_b32_e32 v62, v171
	v_mov_b32_e32 v63, v171
	v_mov_b32_e32 v64, v171
	v_mov_b32_e32 v65, v171
	v_mov_b32_e32 v66, v171
	v_mov_b32_e32 v67, v171
	v_mov_b32_e32 v68, v171
	v_mov_b32_e32 v69, v171
	v_mov_b32_e32 v70, v171
	v_mov_b32_e32 v71, v171
	v_mov_b32_e32 v72, v171
	v_mov_b32_e32 v73, v171
	v_mov_b32_e32 v74, v171
	v_mov_b32_e32 v75, v171
	v_mov_b32_e32 v76, v171
	v_mov_b32_e32 v77, v171
	v_mov_b32_e32 v78, v171
	v_mov_b32_e32 v79, v171
	v_mov_b32_e32 v80, v171
	v_mov_b32_e32 v81, v171
	v_mov_b32_e32 v82, v171
	v_mov_b32_e32 v83, v171
	v_mov_b32_e32 v84, v171
	v_mov_b32_e32 v85, v171
	v_mov_b32_e32 v86, v171
	v_mov_b32_e32 v87, v171
	v_mov_b32_e32 v88, v171
	v_mov_b32_e32 v89, v171
	v_mov_b32_e32 v90, v171
	v_mov_b32_e32 v91, v171
	v_mov_b32_e32 v92, v171
	v_mov_b32_e32 v93, v171
	v_mov_b32_e32 v94, v171
	v_mov_b32_e32 v95, v171
	v_mov_b32_e32 v96, v171
	v_mov_b32_e32 v97, v171
	v_mov_b32_e32 v98, v171
	v_mov_b32_e32 v99, v171
	v_mov_b32_e32 v100, v171
	v_mov_b32_e32 v101, v171
	v_mov_b32_e32 v102, v171
	v_mov_b32_e32 v103, v171
	v_mov_b32_e32 v104, v171
	v_mov_b32_e32 v105, v171
	v_mov_b32_e32 v106, v171
	v_mov_b32_e32 v107, v171
	v_mov_b32_e32 v108, v171
	v_mov_b32_e32 v109, v171
	v_mov_b32_e32 v110, v171
	v_mov_b32_e32 v111, v171
	v_mov_b32_e32 v112, v171
	v_mov_b32_e32 v113, v171
	v_mov_b32_e32 v114, v171
	v_mov_b32_e32 v115, v171
	v_mov_b32_e32 v116, v171
	v_mov_b32_e32 v117, v171
	v_mov_b32_e32 v118, v171
	v_mov_b32_e32 v119, v171
	v_mov_b32_e32 v120, v171
	v_mov_b32_e32 v121, v171
	v_mov_b32_e32 v122, v171
	v_mov_b32_e32 v123, v171
	v_mov_b32_e32 v124, v171
	v_mov_b32_e32 v125, v171
	v_mov_b32_e32 v126, v171
	v_mov_b32_e32 v127, v171
	v_mov_b32_e32 v128, v171
	v_mov_b32_e32 v129, v171
	v_mov_b32_e32 v130, v171
	v_mov_b32_e32 v131, v171
	v_mov_b32_e32 v132, v171
	v_mov_b32_e32 v133, v171
	v_mov_b32_e32 v134, v171
	v_mov_b32_e32 v135, v171
	v_mov_b32_e32 v136, v171
	v_mov_b32_e32 v137, v171
	v_mov_b32_e32 v138, v171
	v_mov_b32_e32 v139, v171
	v_mov_b32_e32 v140, v171
	v_mov_b32_e32 v141, v171
	v_mov_b32_e32 v142, v171
	v_mov_b32_e32 v143, v171
	v_mov_b32_e32 v144, v171
	v_mov_b32_e32 v145, v171
	v_mov_b32_e32 v146, v171
	v_mov_b32_e32 v147, v171
	v_mov_b32_e32 v148, v171
	v_mov_b32_e32 v149, v171
	v_mov_b32_e32 v150, v171
	v_mov_b32_e32 v151, v171
	v_mov_b32_e32 v152, v171
	v_mov_b32_e32 v153, v171
	v_mov_b32_e32 v154, v171
	v_mov_b32_e32 v155, v171
	v_mov_b32_e32 v156, v171
	v_mov_b32_e32 v157, v171
	v_mov_b32_e32 v158, v171
	v_mov_b32_e32 v159, v171
	v_mov_b32_e32 v160, v171
	v_mov_b32_e32 v161, v171
	s_barrier
	s_branch .LBB0_3052

; #define GAS __attribute__((address_space(1)))
; #define PG8_STAGE(bufoff, gbase, voff) do { _Pragma("unroll") for (int _i = 0; _i < 2; ++_i) \
;         __builtin_amdgcn_global_load_lds((const GAS unsigned*)((const GAS char*)(gbase) + (voff)[_i]), (LAS unsigned*)(lds + (bufoff) + ldsw + _i * 8192), 16, 0, 0); } while (0)
; #define PG8_WAIT_V(n) asm volatile("s_waitcnt vmcnt(" #n ")" ::: "memory")
; #define PG8_BAR __builtin_amdgcn_s_barrier()
; #define PG8_OFFS(u, ao, bo) do { _Pragma("unroll") for (int _i = 0; _i < 2; ++_i) { (bo)[_i] = (unsigned)(sRb[_i] * (u).ldb + sC2[_i]); \
;         _Pragma("unroll") for (int _h = 0; _h < 2; ++_h) { int _r = _h * HALF + sR[_i]; if (GATHER) { _r = (u).gl ? (u).gl[_r] : ((_r < (u).gcnt) ? (u).gidx[_r] : 0); } (ao)[_h][_i] = (unsigned)(_r * (u).lda + sC2[_i]); } } } while (0)
; template <class Epi, class Sched, bool GATHER, bool FP8 = false, bool UNI = false>
; __device__ __forceinline__ void gemm_phase(LAS unsigned char* lds, const Sched& S, const Epi& E) {
;     ...
;     const int aoff = lds_byte(wr * 64 + fr, fq * 8), boff = lds_byte(wc * 32 + fr, fq * 8);
;     const int sclw = 0x79, scla = 0x7f;
;     const int aoff8[2] = {lds_byte(wr * 64 + fr, fq * 16), lds_byte(wr * 64 + fr, fq * 16 + 8)}, boff8[2] = {lds_byte(wc * 32 + fr, fq * 16), lds_byte(wc * 32 + fr, fq * 16 + 8)};
;     ...
;     Unit cur, nxt; int ui = 0;
;     if (!S.next(0, cur)) return;
;     f32x4 acc[2][2][4][2];
; #pragma unroll
;     for (int a = 0; a < 2; ++a)
; #pragma unroll
;         for (int b = 0; b < 2; ++b)
; #pragma unroll
;             for (int m = 0; m < 4; ++m)
; #pragma unroll
;                 for (int n = 0; n < 2; ++n) acc[a][b][m][n] = (f32x4){0.f, 0.f, 0.f, 0.f};
;     i32x8 At[4], B0[2], B1[2];
;     unsigned aoc[2][2], boc[2], aon[2][2], bon[2];
;     PG8_OFFS(cur, aoc, boc);
;     {
;         const GAS char* cA = cur.a; const GAS char* cB = cur.b; const size_t hB = (size_t)(Epi::WIDE ? 32 : HALF) * cur.ldb;
;         PG8_STAGE(PG8_SB(0, 0), cB, boc); PG8_STAGE(PG8_SB(0, 1), cB + hB, boc); PG8_STAGE(PG8_SA(0, 0), cA, aoc[0]); PG8_STAGE(PG8_SA(0, 1), cA, aoc[1]);
;         if (wr == 1) PG8_BAR;
;         PG8_WAIT_V(2); PG8_BAR;
;         PG8_STAGE(PG8_SB(1, 0), cB + 128, boc); PG8_STAGE(PG8_SA(1, 0), cA + 128, aoc[0]); PG8_STAGE(PG8_SB(1, 1), cB + hB + 128, boc);
;         PG8_WAIT_V(6); PG8_BAR;
.LBB0_3172:
	s_lshl_b32 s68, s12, 8
	s_lshl_b32 s69, s10, 8
	s_and_b32 s29, s15, 3
	s_lshl_b32 s49, s19, 6
	s_add_u32 s8, s8, 0x3fb00000
	s_addc_u32 s9, s9, 0
	s_add_i32 s30, s16, 0x18000
	s_add_i32 s50, s30, s26
	s_mov_b64 s[10:11], 0x80
	v_lshl_add_u64 v[8:9], v[8:9], 0, s[10:11]
	s_mov_b32 m0, s50
	s_add_i32 s51, s50, 0x2000
	s_add_i32 s56, s45, 0x8000
	s_add_i32 s57, s45, 0xa000
	s_waitcnt vmcnt(2)
	s_barrier
	global_load_lds_dwordx4 v[8:9], off
	v_lshl_add_u64 v[6:7], v[6:7], 0, s[10:11]
	s_mov_b32 m0, s51
	s_add_u32 s12, s22, 0x4080
	global_load_lds_dwordx4 v[6:7], off
	v_lshl_add_u64 v[2:3], v[2:3], 0, s[10:11]
	s_mov_b32 m0, s56
	s_addc_u32 s13, s23, 0
	s_add_i32 s31, s16, 0x1c000
	global_load_lds_dwordx4 v[2:3], off
	v_lshl_add_u64 v[2:3], v[4:5], 0, s[10:11]
	s_mov_b32 m0, s57
	s_add_i32 s58, s31, s26
	global_load_lds_dwordx4 v[2:3], off
	v_lshl_add_u64 v[2:3], s[12:13], 0, v[162:163]
	s_mov_b32 m0, s58
	s_add_i32 s59, s58, 0x2000
	global_load_lds_dwordx4 v[2:3], off
	v_lshl_add_u64 v[2:3], s[12:13], 0, v[168:169]
	s_mov_b32 m0, s59
	v_lshlrev_b32_e32 v5, 1, v1
	global_load_lds_dwordx4 v[2:3], off
	v_lshlrev_b32_e32 v3, 6, v1
	s_cmpk_lt_u32 s14, 0x100
	v_and_b32_e32 v3, 0x3c0, v3
	v_lshlrev_b32_e32 v4, 2, v1
	v_and_b32_e32 v5, 32, v5
	v_lshlrev_b32_e32 v7, 5, v1
	s_cselect_b64 s[12:13], -1, 0
	s_lshl_b32 s14, s15, 11
	v_and_b32_e32 v4, 32, v4
	v_or_b32_e32 v6, v3, v5
	v_and_b32_e32 v7, 0x400, v7
	s_add_i32 s14, s16, s14
	v_lshrrev_b32_e32 v2, 1, v1
	v_lshl_or_b32 v8, s19, 13, v7
	v_bitop3_b32 v5, v3, v4, v5 bitop3:0x36
	v_bitop3_b32 v4, v6, v4, 16 bitop3:0x36
	v_lshl_or_b32 v7, s29, 12, v7
	s_waitcnt vmcnt(6)
	s_add_i32 s14, s14, 0x20000
	s_lshl_b32 s60, s29, 6
	v_bfe_u32 v174, v1, 2, 4
	s_add_i32 s61, s16, 0x24104
	s_ashr_i32 s62, s17, 3
	s_and_b32 s63, s18, 7
	s_ashr_i32 s64, s18, 3
	v_and_b32_e32 v2, 24, v2
	v_or_b32_e32 v9, v5, v8
	v_or_b32_e32 v6, v4, v8
	v_or_b32_e32 v5, v5, v7
	v_or_b32_e32 v4, v4, v7
	v_and_b32_e32 v176, 48, v10
	v_add_u32_e32 v3, s14, v3
	v_lshl_add_u32 v7, v174, 6, s14
	s_cmp_lt_i32 s64, s62
	v_mov_b32_e32 v167, v163
	v_mov_b32_e32 v173, v163
	v_mov_b32_e32 v175, v163
	v_mov_b32_e32 v177, v163
	s_mov_b32 s65, 0
	s_cselect_b64 s[14:15], -1, 0
	v_add_u32_e32 v1, s27, v5
	v_add_u32_e32 v186, s27, v4
	v_add_u32_e32 v187, s28, v5
	v_add_u32_e32 v188, s28, v4
	v_add_u32_e32 v189, s16, v9
	v_add_u32_e32 v190, s16, v6
	v_mov_b32_e32 v191, 0x79
	v_mov_b32_e32 v192, 0x7f
	v_add_u32_e32 v193, s30, v5
	v_add_u32_e32 v194, s30, v4
	v_add_u32_e32 v195, s31, v5
	v_add_u32_e32 v196, s31, v4
	v_mbcnt_lo_u32_b32 v255, -1, 0
	v_mbcnt_hi_u32_b32 v255, -1, v255
	v_and_b32_e32 v255, 16, v255
	v_xor_b32_e32 v1, v1, v255
	v_xor_b32_e32 v186, v186, v255
	v_xor_b32_e32 v187, v187, v255
	v_xor_b32_e32 v188, v188, v255
	v_xor_b32_e32 v189, v189, v255
	v_xor_b32_e32 v190, v190, v255
	v_xor_b32_e32 v193, v193, v255
	v_xor_b32_e32 v194, v194, v255
	v_xor_b32_e32 v195, v195, v255
	v_xor_b32_e32 v196, v196, v255
	v_add_u32_e32 v197, v3, v2
	v_add_u32_e32 v198, v7, v176
	s_barrier
	s_branch .LBB0_3175

; #define GAS __attribute__((address_space(1)))
; #define LAS __attribute__((address_space(3)))
; __global__ void __launch_bounds__(512, 2) kfwd(Args args) {
;     extern __shared__ __attribute__((aligned(16))) unsigned char lds_raw[];
;     Frame F0;
;     F0.lds = (LAS unsigned char*)lds_raw;
;     F0.G = gridDim.x; F0.bid = blockIdx.x; F0.ws = (GAS unsigned char*)args.ws; F0.ctl = (GAS unsigned*)(args.ws + WS_CTL);
;     for (int u = threadIdx.x; u < (LDS_BYTES - LDS_TAB) / 4; u += 512) ((LAS unsigned*)(F0.lds + LDS_TAB))[u] = 0u;
;     __syncthreads();
;     XcdBarrier bar = xcd_barrier_post((unsigned*)(F0.ctl + CW_BAR), (volatile LAS unsigned*)(F0.lds + LDS_MISC));
;     const int lo = args.ph_lo, hi = args.ph_hi;
;     if (PROBE_MASK != 0 && threadIdx.x == 0) ((LAS unsigned long long*)(F0.lds + LDS_STAMP))[0] = __builtin_amdgcn_s_memrealtime();
;     run_layer<0>(F0, bar, lo, hi);
;     run_layer<1>(F0, bar, lo, hi);
;     if (PROBE_MASK != 0 && blockIdx.x == 0 && threadIdx.x == 0) {
;         const LAS unsigned long long* ts = (const LAS unsigned long long*)(F0.lds + LDS_STAMP); unsigned long long tot = 0;
;         for (int k = 0; k < N_PHASES; ++k) if ((PROBE_MASK >> (k % PH_PER_LAYER)) & 1) tot += ts[k + 1] - ts[k];
;         const unsigned long long t0 = __builtin_amdgcn_s_memrealtime(), lim = tot * PROBE_AMP < 4000000ull ? tot * PROBE_AMP : 4000000ull;
;         while (__builtin_amdgcn_s_memrealtime() - t0 < lim) __builtin_amdgcn_s_sleep(32);
;     }
; }
	.amdhsa_kernel _Z4kfwd4Args
		.amdhsa_group_segment_fixed_size 0
		.amdhsa_private_segment_fixed_size 0
		.amdhsa_kernarg_size 440
		.amdhsa_user_sgpr_count 2
		.amdhsa_user_sgpr_dispatch_ptr 0
		.amdhsa_user_sgpr_queue_ptr 0
		.amdhsa_user_sgpr_kernarg_segment_ptr 1
		.amdhsa_user_sgpr_dispatch_id 0
		.amdhsa_user_sgpr_kernarg_preload_length 0
		.amdhsa_user_sgpr_kernarg_preload_offset 0
		.amdhsa_user_sgpr_private_segment_size 0
		.amdhsa_uses_dynamic_stack 0
		.amdhsa_enable_private_segment 0
		.amdhsa_system_sgpr_workgroup_id_x 1
		.amdhsa_system_sgpr_workgroup_id_y 0
		.amdhsa_system_sgpr_workgroup_id_z 0
		.amdhsa_system_sgpr_workgroup_info 0
		.amdhsa_system_vgpr_workitem_id 0
		.amdhsa_next_free_vgpr 256
		.amdhsa_next_free_sgpr 98
		.amdhsa_accum_offset 256
		.amdhsa_reserve_vcc 1
		.amdhsa_float_round_mode_32 0
		.amdhsa_float_round_mode_16_64 0
		.amdhsa_float_denorm_mode_32 3
		.amdhsa_float_denorm_mode_16_64 3
		.amdhsa_dx10_clamp 1
		.amdhsa_ieee_mode 1
		.amdhsa_fp16_overflow 0
		.amdhsa_tg_split 0
		.amdhsa_exception_fp_ieee_invalid_op 0
		.amdhsa_exception_fp_denorm_src 0
		.amdhsa_exception_fp_ieee_div_zero 0
		.amdhsa_exception_fp_ieee_overflow 0
		.amdhsa_exception_fp_ieee_underflow 0
		.amdhsa_exception_fp_ieee_inexact 0
		.amdhsa_exception_int_div_zero 0
	.end_amdhsa_kernel

; #define GAS __attribute__((address_space(1)))
; #define LAS __attribute__((address_space(3)))
; __global__ void __launch_bounds__(512, 2) kfwd(Args args) {
;     extern __shared__ __attribute__((aligned(16))) unsigned char lds_raw[];
;     Frame F0;
;     F0.lds = (LAS unsigned char*)lds_raw;
;     F0.G = gridDim.x; F0.bid = blockIdx.x; F0.ws = (GAS unsigned char*)args.ws; F0.ctl = (GAS unsigned*)(args.ws + WS_CTL);
;     for (int u = threadIdx.x; u < (LDS_BYTES - LDS_TAB) / 4; u += 512) ((LAS unsigned*)(F0.lds + LDS_TAB))[u] = 0u;
;     __syncthreads();
;     XcdBarrier bar = xcd_barrier_post((unsigned*)(F0.ctl + CW_BAR), (volatile LAS unsigned*)(F0.lds + LDS_MISC));
;     const int lo = args.ph_lo, hi = args.ph_hi;
;     if (PROBE_MASK != 0 && threadIdx.x == 0) ((LAS unsigned long long*)(F0.lds + LDS_STAMP))[0] = __builtin_amdgcn_s_memrealtime();
;     run_layer<0>(F0, bar, lo, hi);
;     run_layer<1>(F0, bar, lo, hi);
;     if (PROBE_MASK != 0 && blockIdx.x == 0 && threadIdx.x == 0) {
;         const LAS unsigned long long* ts = (const LAS unsigned long long*)(F0.lds + LDS_STAMP); unsigned long long tot = 0;
;         for (int k = 0; k < N_PHASES; ++k) if ((PROBE_MASK >> (k % PH_PER_LAYER)) & 1) tot += ts[k + 1] - ts[k];
;         const unsigned long long t0 = __builtin_amdgcn_s_memrealtime(), lim = tot * PROBE_AMP < 4000000ull ? tot * PROBE_AMP : 4000000ull;
;         while (__builtin_amdgcn_s_memrealtime() - t0 < lim) __builtin_amdgcn_s_sleep(32);
;     }
; }
amdhsa.kernels:
  - .agpr_count:     0
    .args:
      - .offset:         0
        .size:           184
        .value_kind:     by_value
      - .offset:         184
        .size:           4
        .value_kind:     hidden_block_count_x
      - .offset:         188
        .size:           4
        .value_kind:     hidden_block_count_y
      - .offset:         192
        .size:           4
        .value_kind:     hidden_block_count_z
      - .offset:         196
        .size:           2
        .value_kind:     hidden_group_size_x
      - .offset:         198
        .size:           2
        .value_kind:     hidden_group_size_y
      - .offset:         200
        .size:           2
        .value_kind:     hidden_group_size_z
      - .offset:         202
        .size:           2
        .value_kind:     hidden_remainder_x
      - .offset:         204
        .size:           2
        .value_kind:     hidden_remainder_y
      - .offset:         206
        .size:           2
        .value_kind:     hidden_remainder_z
      - .offset:         224
        .size:           8
        .value_kind:     hidden_global_offset_x
      - .offset:         232
        .size:           8
        .value_kind:     hidden_global_offset_y
      - .offset:         240
        .size:           8
        .value_kind:     hidden_global_offset_z
      - .offset:         248
        .size:           2
        .value_kind:     hidden_grid_dims
      - .offset:         304
        .size:           4
        .value_kind:     hidden_dynamic_lds_size
    .group_segment_fixed_size: 0
    .kernarg_segment_align: 8
    .kernarg_segment_size: 440
    .language:       OpenCL C
    .language_version:
      - 2
      - 0
    .max_flat_workgroup_size: 512
    .name:           _Z4kfwd4Args
    .private_segment_fixed_size: 0
    .sgpr_count:     104
    .sgpr_spill_count: 92
    .symbol:         _Z4kfwd4Args.kd
    .uniform_work_group_size: 1
    .uses_dynamic_stack: false
    .vgpr_count:     256
    .vgpr_spill_count: 0
    .wavefront_size: 64
